# v19
# baseline (speedup 1.0000x reference)
_Z12gemm_persistILi0ELi4096ELi32ELi112EEvPKDF16_S1_PvPKfS4_S4_S4_PDF16_S5_iii:
	s_load_dwordx4 s[16:19], s[0:1], 0x48
	s_load_dword s3, s[0:1], 0x58
	s_waitcnt lgkmcnt(0)
	v_readfirstlane_b32 s19, v0
	s_mul_i32 s4, s3, s17
	s_add_i32 s4, s4, s2
	s_cmpk_gt_i32 s4, 0xdff
	s_cbranch_scc1 .LBB1_30
	v_lshrrev_b32_e32 v1, 5, v0
	v_lshrrev_b32_e32 v4, 2, v0
	v_and_b32_e32 v1, 4, v1
	v_lshrrev_b32_e32 v2, 3, v0
	v_bfe_u32 v3, v0, 3, 2
	v_and_b32_e32 v4, 24, v4
	v_or3_b32 v3, v1, v3, v4
	v_or_b32_e32 v4, 64, v2
	s_movk_i32 s5, 0x60
	v_and_or_b32 v5, v4, s5, v3
	s_ashr_i32 s5, s4, 31
	s_lshr_b32 s5, s5, 29
	s_add_i32 s5, s4, s5
	s_lshr_b32 s30, s19, 6
	s_ashr_i32 s8, s5, 3
	s_and_b32 s5, s5, -8
	s_lshr_b32 s31, s19, 8
	s_lshl_b32 s10, s30, 10
	s_sub_i32 s4, s4, s5
	s_cmp_lt_i32 s4, 0
	s_movk_i32 s33, 0x1c1
	s_cselect_b32 s5, s33, 0x1c0
	s_mul_i32 s4, s5, s4
	s_add_i32 s4, s4, s8
	s_mul_hi_i32 s5, s4, 0x92492493
	s_add_i32 s5, s5, s4
	s_lshr_b32 s8, s5, 31
	s_ashr_i32 s5, s5, 9
	s_add_i32 s5, s5, s8
	s_lshl_b32 s8, s5, 3
	s_mulk_i32 s5, 0x380
	s_sub_i32 s4, s4, s5
	s_bfe_u32 s5, s4, 0x3001c
	s_add_i32 s5, s4, s5
	s_sext_i32_i16 s9, s5
	s_and_b32 s5, s5, 0xfff8
	s_sub_i32 s4, s4, s5
	s_load_dwordx4 s[20:23], s[0:1], 0x0
	s_load_dwordx2 s[6:7], s[0:1], 0x10
	s_sext_i32_i16 s4, s4
	s_lshr_b32 s28, s9, 3
	s_add_i32 s42, s8, s4
	s_ashr_i32 s43, s42, 31
	s_bfe_i64 s[4:5], s[28:29], 0x100000
	s_lshl_b64 s[8:9], s[42:43], 21
	s_lshl_b64 s[4:5], s[4:5], 21
	v_xor_b32_e32 v1, v2, v0
	s_waitcnt lgkmcnt(0)
	s_add_u32 s4, s22, s4
	v_lshlrev_b32_e32 v1, 4, v1
	s_addc_u32 s5, s23, s5
	s_add_i32 s43, s10, 0
	v_and_b32_e32 v1, 0x70, v1
	v_and_or_b32 v3, v2, 32, v3
	s_add_i32 s52, s43, 0x10000
	s_add_i32 s53, s43, 0x12000
	v_lshl_or_b32 v200, v3, 13, v1
	s_mov_b32 m0, s52
	s_add_u32 s44, s20, s8
	v_lshl_or_b32 v196, v5, 13, v1
	v_lshlrev_b32_e32 v2, 13, v2
	global_load_lds_dwordx4 v200, s[4:5] sc1
	s_mov_b32 m0, s53
	s_addc_u32 s45, s21, s9
	s_add_i32 s54, s43, 0x2000
	v_or_b32_e32 v202, v2, v1
	global_load_lds_dwordx4 v196, s[4:5] sc1
	s_mov_b32 m0, s43
	s_add_u32 s8, s4, 0x100000
	v_lshl_or_b32 v198, v4, 13, v1
	global_load_lds_dwordx4 v202, s[44:45] sc1
	s_mov_b32 m0, s54
	s_addc_u32 s9, s5, 0
	s_add_i32 s55, s43, 0x14000
	global_load_lds_dwordx4 v198, s[44:45] sc1
	s_mov_b32 m0, s55
	s_add_i32 s56, s43, 0x16000
	global_load_lds_dwordx4 v200, s[8:9] sc1
	s_mov_b32 m0, s56
	v_mov_b32_e32 v205, 0
	global_load_lds_dwordx4 v196, s[8:9] sc1
	s_add_u32 s8, s44, 0x100000
	s_addc_u32 s9, s45, 0
	s_add_i32 s57, s43, 0x4000
	v_mov_b32_e32 v201, v205
	s_mov_b32 m0, s57
	s_add_i32 s58, s43, 0x6000
	v_lshl_add_u64 v[4:5], s[4:5], 0, v[200:201]
	v_mov_b32_e32 v197, v205
	global_load_lds_dwordx4 v202, s[8:9] sc1
	s_mov_b32 m0, s58
	s_add_i32 s59, s43, 0x18000
	s_mov_b64 s[24:25], 0x80
	v_lshl_add_u64 v[6:7], s[4:5], 0, v[196:197]
	v_mov_b32_e32 v203, v205
	global_load_lds_dwordx4 v198, s[8:9] sc1
	v_lshl_add_u64 v[4:5], v[4:5], 0, s[24:25]
	s_mov_b32 m0, s59
	s_add_i32 s60, s43, 0x1a000
	v_lshl_add_u64 v[8:9], s[44:45], 0, v[202:203]
	v_mov_b32_e32 v199, v205
	global_load_lds_dwordx4 v[4:5], off sc1
	v_lshl_add_u64 v[4:5], v[6:7], 0, s[24:25]
	s_mov_b32 m0, s60
	s_add_i32 s61, s43, 0x8000
	s_add_i32 s62, s43, 0xa000
	v_lshl_add_u64 v[10:11], s[44:45], 0, v[198:199]
	global_load_lds_dwordx4 v[4:5], off sc1
	v_lshl_add_u64 v[4:5], v[8:9], 0, s[24:25]
	s_mov_b32 m0, s61
	s_add_u32 s8, s4, 0x100080
	global_load_lds_dwordx4 v[4:5], off sc1
	v_lshl_add_u64 v[4:5], v[10:11], 0, s[24:25]
	s_mov_b32 m0, s62
	s_addc_u32 s9, s5, 0
	s_add_i32 s63, s43, 0x1c000
	global_load_lds_dwordx4 v[4:5], off sc1
	s_mov_b32 m0, s63
	s_add_i32 s64, s43, 0x1e000
	global_load_lds_dwordx4 v200, s[8:9] sc1
	s_mov_b32 m0, s64
	s_mov_b32 s29, 0
	global_load_lds_dwordx4 v196, s[8:9] sc1
	s_load_dwordx2 s[26:27], s[0:1], 0x40
	s_load_dwordx8 s[8:15], s[0:1], 0x20
	s_waitcnt vmcnt(6)
	s_cmp_lg_u32 s31, 1
	s_barrier
	s_cbranch_scc1 .LBB1_3
	s_barrier

.LBB1_14:
	ds_read_b128 v[148:151], v228
	ds_read_b128 v[152:155], v229
	ds_read_b128 v[156:159], v228 offset:2048
	ds_read_b128 v[160:163], v229 offset:2048
	s_add_i32 m0, s43, 0xc000
	ds_read_b128 v[132:135], v228 offset:16384
	ds_read_b128 v[136:139], v229 offset:16384
	ds_read_b128 v[140:143], v228 offset:18432
	ds_read_b128 v[144:147], v229 offset:18432
	ds_read_b128 v[166:169], v226
	ds_read_b128 v[170:173], v226 offset:2048
	ds_read_b128 v[174:177], v227
	ds_read_b128 v[178:181], v227 offset:2048
	ds_read_b128 v[182:185], v226 offset:4096
	ds_read_b128 v[186:189], v226 offset:6144
	ds_read_b128 v[190:193], v227 offset:4096
	ds_read_b128 v[214:217], v227 offset:6144
	global_load_lds_dwordx4 v208, s[44:45] sc1
	s_add_i32 m0, s43, 0xe000
	s_nop 0
	global_load_lds_dwordx4 v210, s[44:45] sc1
	s_lshr_b32 s94, s82, 2
	s_add_i32 s94, s94, s79
	s_mov_b64 vcc, s[0:1]
	s_cbranch_vccz .LBB1_26
	s_mul_hi_i32 s95, s94, 0x92492493
	s_add_i32 s95, s95, s94
	s_lshr_b32 s28, s95, 31
	s_ashr_i32 s95, s95, 12
	s_add_i32 s95, s95, s28
	s_mul_i32 s28, s95, 0x1c00
	s_sub_i32 s46, s94, s28
	s_bitcmp0_b32 s95, 0
	s_cselect_b32 s28, s16, 0x2a00
	s_ashr_i32 s49, s46, 1
	s_lshl_b32 s46, s46, 11
	s_add_i32 s28, s28, s49
	s_and_b32 s92, s46, 0x800
	s_cmp_lt_u32 s95, 2
	s_cselect_b32 s50, s9, s11
	s_cselect_b32 s51, s8, s10
	s_lshl_b64 s[46:47], s[28:29], 14
	s_add_u32 s46, s51, s46
	s_addc_u32 s47, s50, s47
	s_lshl_b32 s93, s92, 2
	s_add_u32 s88, s46, s93
	s_addc_u32 s89, s47, 0
	s_lshl_b32 s95, s95, 6
	s_lshl_b32 s28, s28, 1
	s_and_b32 s46, s49, 0x7f
	s_and_b32 s95, s95, 0xffffff80
	s_and_b32 s28, s28, 0x7fffff00
	s_or_b32 s95, s95, s46
	s_add_i32 s46, s95, s28
	s_ashr_i32 s47, s46, 31
	s_lshl_b64 s[46:47], s[46:47], 13
	s_add_u32 s46, s14, s46
	s_addc_u32 s47, s15, s47
	s_lshl_b32 s93, s92, 1
	s_add_u32 s90, s46, s93
	s_addc_u32 s91, s47, 0
	s_branch .LBB1_12

.LBB1_16:
	s_add_u32 s28, s44, 0xfff00080
	s_addc_u32 s46, s45, -1
	s_cmp_eq_u32 s48, 60
	s_cselect_b32 s49, s31, s46
	s_cselect_b32 s47, s35, s81
	s_cselect_b32 s46, s78, s80
	s_mov_b32 m0, s52
	s_cselect_b32 s48, s77, s28
	s_add_u32 s50, s46, 0x100000
	ds_read_b128 v[188:191], v226 offset:16384
	ds_read_b128 v[176:179], v226 offset:18432
	ds_read_b128 v[192:195], v227 offset:16384
	ds_read_b128 v[180:183], v227 offset:18432
	ds_read_b128 v[172:175], v226 offset:20480
	ds_read_b128 v[164:167], v226 offset:22528
	ds_read_b128 v[184:187], v227 offset:20480
	ds_read_b128 v[168:171], v227 offset:22528
	global_load_lds_dwordx4 v200, s[46:47] sc1
	s_mov_b32 m0, s53
	s_addc_u32 s51, s47, 0
	global_load_lds_dwordx4 v196, s[46:47] sc1
	s_mov_b32 m0, s55
	s_add_u32 s84, s46, 0x80
	s_addc_u32 s85, s47, 0
	global_load_lds_dwordx4 v200, s[50:51] sc1
	s_mov_b32 m0, s56
	s_add_u32 s86, s48, 0x80
	s_addc_u32 s87, s49, 0
	s_and_b64 s[4:5], exec, s[4:5]
	global_load_lds_dwordx4 v196, s[50:51] sc1
	s_mov_b32 m0, s43
	s_mov_b64 s[50:51], -1
	global_load_lds_dwordx4 v202, s[48:49] sc1
	s_mov_b32 m0, s54
	s_mov_b64 vcc, s[4:5]
	global_load_lds_dwordx4 v198, s[48:49] sc1
	s_cbranch_vccz .LBB1_18
	s_waitcnt vmcnt(8)
	s_mov_b64 s[50:51], 0

.LBB1_20:
	s_waitcnt lgkmcnt(0)
	s_barrier
	s_setprio 1
	s_waitcnt lgkmcnt(0)
	v_mfma_f32_16x16x32_f16 v[64:67], v[148:151], v[188:191], v[64:67]
	v_mfma_f32_16x16x32_f16 v[64:67], v[152:155], v[192:195], v[64:67]
	v_mfma_f32_16x16x32_f16 v[56:59], v[160:163], v[192:195], v[56:59]
	v_mfma_f32_16x16x32_f16 v[56:59], v[156:159], v[188:191], v[56:59]
	v_mfma_f32_16x16x32_f16 v[40:43], v[156:159], v[176:179], v[40:43]
	v_mfma_f32_16x16x32_f16 v[40:43], v[160:163], v[180:183], v[40:43]
	v_mfma_f32_16x16x32_f16 v[48:51], v[152:155], v[180:183], v[48:51]
	v_mfma_f32_16x16x32_f16 v[48:51], v[148:151], v[176:179], v[48:51]
	v_mfma_f32_16x16x32_f16 v[32:35], v[148:151], v[172:175], v[32:35]
	v_mfma_f32_16x16x32_f16 v[32:35], v[152:155], v[184:187], v[32:35]
	v_mfma_f32_16x16x32_f16 v[24:27], v[160:163], v[184:187], v[24:27]
	v_mfma_f32_16x16x32_f16 v[24:27], v[156:159], v[172:175], v[24:27]
	v_mfma_f32_16x16x32_f16 v[8:11], v[156:159], v[164:167], v[8:11]
	v_mfma_f32_16x16x32_f16 v[8:11], v[160:163], v[168:171], v[8:11]
	v_mfma_f32_16x16x32_f16 v[16:19], v[152:155], v[168:171], v[16:19]
	v_mfma_f32_16x16x32_f16 v[16:19], v[148:151], v[164:167], v[16:19]
	s_setprio 0
	s_setprio 1
	v_mfma_f32_16x16x32_f16 v[60:63], v[132:135], v[188:191], v[60:63]
	v_mfma_f32_16x16x32_f16 v[60:63], v[136:139], v[192:195], v[60:63]
	v_mfma_f32_16x16x32_f16 v[52:55], v[144:147], v[192:195], v[52:55]
	v_mfma_f32_16x16x32_f16 v[52:55], v[140:143], v[188:191], v[52:55]
	v_mfma_f32_16x16x32_f16 v[36:39], v[140:143], v[176:179], v[36:39]
	v_mfma_f32_16x16x32_f16 v[36:39], v[144:147], v[180:183], v[36:39]
	v_mfma_f32_16x16x32_f16 v[44:47], v[136:139], v[180:183], v[44:47]
	v_mfma_f32_16x16x32_f16 v[44:47], v[132:135], v[176:179], v[44:47]
	v_mfma_f32_16x16x32_f16 v[28:31], v[132:135], v[172:175], v[28:31]
	v_mfma_f32_16x16x32_f16 v[28:31], v[136:139], v[184:187], v[28:31]
	v_mfma_f32_16x16x32_f16 v[20:23], v[144:147], v[184:187], v[20:23]
	v_mfma_f32_16x16x32_f16 v[20:23], v[140:143], v[172:175], v[20:23]
	v_mfma_f32_16x16x32_f16 v[4:7], v[140:143], v[164:167], v[4:7]
	v_mfma_f32_16x16x32_f16 v[4:7], v[144:147], v[168:171], v[4:7]
	v_mfma_f32_16x16x32_f16 v[12:15], v[136:139], v[168:171], v[12:15]
	v_mfma_f32_16x16x32_f16 v[12:15], v[132:135], v[164:167], v[12:15]
	s_setprio 0
	s_barrier
	s_add_u32 s48, s48, 0x100000
	ds_read_b128 v[148:151], v228 offset:32768
	ds_read_b128 v[152:155], v229 offset:32768
	s_addc_u32 s49, s49, 0
	s_mov_b32 m0, s57
	ds_read_b128 v[156:159], v228 offset:34816
	ds_read_b128 v[160:163], v229 offset:34816
	ds_read_b128 v[132:135], v228 offset:49152
	ds_read_b128 v[136:139], v229 offset:49152
	ds_read_b128 v[140:143], v228 offset:51200
	ds_read_b128 v[144:147], v229 offset:51200
	ds_read_b128 v[188:191], v226 offset:32768
	ds_read_b128 v[176:179], v226 offset:34816
	ds_read_b128 v[192:195], v227 offset:32768
	ds_read_b128 v[180:183], v227 offset:34816
	ds_read_b128 v[172:175], v226 offset:36864
	ds_read_b128 v[164:167], v226 offset:38912
	ds_read_b128 v[184:187], v227 offset:36864
	ds_read_b128 v[168:171], v227 offset:38912
	global_load_lds_dwordx4 v202, s[48:49] sc1
	s_mov_b32 m0, s58
	s_nop 0
	global_load_lds_dwordx4 v198, s[48:49] sc1
	s_mov_b64 s[48:49], -1
	s_mov_b64 vcc, s[4:5]
	s_cbranch_vccz .LBB1_22
	s_waitcnt vmcnt(8)
	s_mov_b64 s[48:49], 0

.LBB1_24:
	s_waitcnt lgkmcnt(0)
	s_barrier
	s_setprio 1
	s_waitcnt lgkmcnt(0)
	v_mfma_f32_16x16x32_f16 v[128:131], v[148:151], v[188:191], v[128:131]
	v_mfma_f32_16x16x32_f16 v[128:131], v[152:155], v[192:195], v[128:131]
	v_mfma_f32_16x16x32_f16 v[120:123], v[160:163], v[192:195], v[120:123]
	v_mfma_f32_16x16x32_f16 v[120:123], v[156:159], v[188:191], v[120:123]
	v_mfma_f32_16x16x32_f16 v[104:107], v[156:159], v[176:179], v[104:107]
	v_mfma_f32_16x16x32_f16 v[104:107], v[160:163], v[180:183], v[104:107]
	v_mfma_f32_16x16x32_f16 v[112:115], v[152:155], v[180:183], v[112:115]
	v_mfma_f32_16x16x32_f16 v[112:115], v[148:151], v[176:179], v[112:115]
	v_mfma_f32_16x16x32_f16 v[96:99], v[148:151], v[172:175], v[96:99]
	v_mfma_f32_16x16x32_f16 v[96:99], v[152:155], v[184:187], v[96:99]
	v_mfma_f32_16x16x32_f16 v[88:91], v[160:163], v[184:187], v[88:91]
	v_mfma_f32_16x16x32_f16 v[88:91], v[156:159], v[172:175], v[88:91]
	v_mfma_f32_16x16x32_f16 v[72:75], v[156:159], v[164:167], v[72:75]
	v_mfma_f32_16x16x32_f16 v[72:75], v[160:163], v[168:171], v[72:75]
	v_mfma_f32_16x16x32_f16 v[80:83], v[152:155], v[168:171], v[80:83]
	v_mfma_f32_16x16x32_f16 v[80:83], v[148:151], v[164:167], v[80:83]
	s_setprio 0
	s_setprio 1
	v_mfma_f32_16x16x32_f16 v[124:127], v[132:135], v[188:191], v[124:127]
	v_mfma_f32_16x16x32_f16 v[124:127], v[136:139], v[192:195], v[124:127]
	v_mfma_f32_16x16x32_f16 v[116:119], v[144:147], v[192:195], v[116:119]
	v_mfma_f32_16x16x32_f16 v[116:119], v[140:143], v[188:191], v[116:119]
	v_mfma_f32_16x16x32_f16 v[100:103], v[140:143], v[176:179], v[100:103]
	v_mfma_f32_16x16x32_f16 v[100:103], v[144:147], v[180:183], v[100:103]
	v_mfma_f32_16x16x32_f16 v[108:111], v[136:139], v[180:183], v[108:111]
	v_mfma_f32_16x16x32_f16 v[108:111], v[132:135], v[176:179], v[108:111]
	v_mfma_f32_16x16x32_f16 v[92:95], v[132:135], v[172:175], v[92:95]
	v_mfma_f32_16x16x32_f16 v[92:95], v[136:139], v[184:187], v[92:95]
	v_mfma_f32_16x16x32_f16 v[84:87], v[144:147], v[184:187], v[84:87]
	v_mfma_f32_16x16x32_f16 v[84:87], v[140:143], v[172:175], v[84:87]
	v_mfma_f32_16x16x32_f16 v[68:71], v[140:143], v[164:167], v[68:71]
	v_mfma_f32_16x16x32_f16 v[68:71], v[144:147], v[168:171], v[68:71]
	v_mfma_f32_16x16x32_f16 v[76:79], v[136:139], v[168:171], v[76:79]
	v_mfma_f32_16x16x32_f16 v[76:79], v[132:135], v[164:167], v[76:79]
	s_setprio 0
	s_barrier
	s_mov_b32 m0, s59
	s_add_u32 s4, s46, 0x100080
	ds_read_b128 v[164:167], v226 offset:49152
	ds_read_b128 v[168:171], v226 offset:51200
	ds_read_b128 v[172:175], v227 offset:49152
	ds_read_b128 v[176:179], v227 offset:51200
	ds_read_b128 v[180:183], v226 offset:53248
	ds_read_b128 v[184:187], v226 offset:55296
	ds_read_b128 v[188:191], v227 offset:53248
	ds_read_b128 v[192:195], v227 offset:55296
	global_load_lds_dwordx4 v200, s[84:85] sc1
	s_mov_b32 m0, s60
	s_addc_u32 s5, s47, 0
	global_load_lds_dwordx4 v196, s[84:85] sc1
	s_mov_b32 m0, s63
	s_nop 0
	global_load_lds_dwordx4 v200, s[4:5] sc1
	s_mov_b32 m0, s64
	s_nop 0
	global_load_lds_dwordx4 v196, s[4:5] sc1
	s_mov_b32 m0, s61
	s_nop 0
	global_load_lds_dwordx4 v202, s[86:87] sc1
	s_mov_b32 m0, s62
	s_nop 0
	global_load_lds_dwordx4 v198, s[86:87] sc1
	s_waitcnt vmcnt(8)
	s_waitcnt lgkmcnt(0)
	s_barrier
	s_setprio 1
	s_waitcnt lgkmcnt(0)
	v_mfma_f32_16x16x32_f16 v[64:67], v[148:151], v[164:167], v[64:67]
	v_mfma_f32_16x16x32_f16 v[64:67], v[152:155], v[172:175], v[64:67]
	v_mfma_f32_16x16x32_f16 v[56:59], v[160:163], v[172:175], v[56:59]
	v_mfma_f32_16x16x32_f16 v[56:59], v[156:159], v[164:167], v[56:59]
	v_mfma_f32_16x16x32_f16 v[40:43], v[156:159], v[168:171], v[40:43]
	v_mfma_f32_16x16x32_f16 v[40:43], v[160:163], v[176:179], v[40:43]
	v_mfma_f32_16x16x32_f16 v[48:51], v[152:155], v[176:179], v[48:51]
	v_mfma_f32_16x16x32_f16 v[48:51], v[148:151], v[168:171], v[48:51]
	v_mfma_f32_16x16x32_f16 v[32:35], v[148:151], v[180:183], v[32:35]
	v_mfma_f32_16x16x32_f16 v[32:35], v[152:155], v[188:191], v[32:35]
	v_mfma_f32_16x16x32_f16 v[24:27], v[160:163], v[188:191], v[24:27]
	v_mfma_f32_16x16x32_f16 v[24:27], v[156:159], v[180:183], v[24:27]
	v_mfma_f32_16x16x32_f16 v[8:11], v[156:159], v[184:187], v[8:11]
	v_mfma_f32_16x16x32_f16 v[8:11], v[160:163], v[192:195], v[8:11]
	v_mfma_f32_16x16x32_f16 v[16:19], v[152:155], v[192:195], v[16:19]
	v_mfma_f32_16x16x32_f16 v[16:19], v[148:151], v[184:187], v[16:19]
	s_setprio 0
	s_setprio 1
	v_mfma_f32_16x16x32_f16 v[60:63], v[132:135], v[164:167], v[60:63]
	v_mfma_f32_16x16x32_f16 v[60:63], v[136:139], v[172:175], v[60:63]
	v_mfma_f32_16x16x32_f16 v[52:55], v[144:147], v[172:175], v[52:55]
	v_mfma_f32_16x16x32_f16 v[52:55], v[140:143], v[164:167], v[52:55]
	v_mfma_f32_16x16x32_f16 v[36:39], v[140:143], v[168:171], v[36:39]
	v_mfma_f32_16x16x32_f16 v[36:39], v[144:147], v[176:179], v[36:39]
	v_mfma_f32_16x16x32_f16 v[44:47], v[136:139], v[176:179], v[44:47]
	v_mfma_f32_16x16x32_f16 v[44:47], v[132:135], v[168:171], v[44:47]
	v_mfma_f32_16x16x32_f16 v[28:31], v[132:135], v[180:183], v[28:31]
	v_mfma_f32_16x16x32_f16 v[28:31], v[136:139], v[188:191], v[28:31]
	v_mfma_f32_16x16x32_f16 v[20:23], v[144:147], v[188:191], v[20:23]
	v_mfma_f32_16x16x32_f16 v[20:23], v[140:143], v[180:183], v[20:23]
	v_mfma_f32_16x16x32_f16 v[4:7], v[140:143], v[184:187], v[4:7]
	v_mfma_f32_16x16x32_f16 v[4:7], v[144:147], v[192:195], v[4:7]
	v_mfma_f32_16x16x32_f16 v[12:15], v[136:139], v[192:195], v[12:15]
	v_mfma_f32_16x16x32_f16 v[12:15], v[132:135], v[184:187], v[12:15]
	s_setprio 0
	s_barrier
	s_add_u32 s80, s80, 0x100
	s_addc_u32 s81, s81, 0
	s_add_u32 s44, s44, 0x100
	s_addc_u32 s45, s45, 0
	s_cmp_gt_u32 s82, 61
	s_cbranch_scc1 .LBB1_4
	s_mov_b32 s48, s82
	s_branch .LBB1_9

.LBB2_5:
	s_add_i32 s8, s10, s8
	s_ashr_i32 s9, s8, 31
	s_lshr_b32 s9, s9, 25
	s_add_i32 s9, s8, s9
	s_ashr_i32 s10, s9, 7
	s_and_b32 s9, s9, 0xff80
	s_sub_i32 s8, s8, s9
	s_bfe_i32 s9, s8, 0x80000
	s_bfe_u32 s9, s9, 0x3000c
	s_add_i32 s9, s8, s9
	s_bfe_i32 s11, s9, 0x80000
	s_and_b32 s9, s9, 0xf8
	s_sub_i32 s8, s8, s9
	v_lshrrev_b32_e32 v2, 3, v0
	s_lshl_b32 s10, s10, 3
	s_sext_i32_i16 s11, s11
	s_sext_i32_i8 s8, s8
	v_xor_b32_e32 v1, v2, v0
	s_lshr_b32 s17, s33, 6
	s_add_i32 s55, s10, s8
	s_ashr_i32 s10, s11, 3
	s_lshr_b32 s16, s33, 8
	v_lshlrev_b32_e32 v3, 3, v1
	s_lshl_b32 s36, s17, 10
	s_lshr_b32 s18, s11, 3
	s_mul_hi_i32 s11, s10, 0x700000
	s_mul_i32 s10, s10, 0x700000
	v_and_b32_e32 v3, 56, v3
	v_mul_u32_u24_e32 v2, 0x3800, v2
	s_waitcnt lgkmcnt(0)
	s_add_u32 s28, s6, s10
	v_or_b32_e32 v4, v2, v3
	s_addc_u32 s29, s7, s11
	s_add_i32 s37, s36, 0
	v_lshlrev_b32_e32 v128, 1, v4
	s_add_i32 m0, s37, 0x10000
	s_mul_i32 s9, s55, 0x700000
	global_load_lds_dwordx4 v128, s[28:29] sc1
	s_add_i32 m0, s37, 0x12000
	v_add_u32_e32 v130, 0x1c0000, v128
	s_mul_hi_i32 s8, s55, 0x700000
	s_add_u32 s30, s4, s9
	global_load_lds_dwordx4 v130, s[28:29] sc1
	s_addc_u32 s31, s5, s8
	s_mov_b32 m0, s37
	s_add_i32 s38, s37, 0x2000
	global_load_lds_dwordx4 v128, s[30:31] sc1
	s_mov_b32 m0, s38
	s_add_u32 s8, s28, 0x380000
	global_load_lds_dwordx4 v130, s[30:31] sc1
	s_addc_u32 s9, s29, 0
	s_add_i32 m0, s37, 0x14000
	v_mov_b32_e32 v129, 0
	global_load_lds_dwordx4 v128, s[8:9] sc1
	s_add_i32 m0, s37, 0x16000
	v_lshl_add_u64 v[4:5], s[28:29], 0, v[128:129]
	global_load_lds_dwordx4 v130, s[8:9] sc1
	s_add_u32 s8, s30, 0x380000
	s_addc_u32 s9, s31, 0
	s_add_i32 s39, s37, 0x4000
	s_mov_b32 m0, s39
	s_add_i32 s40, s37, 0x6000
	v_mov_b32_e32 v131, v129
	global_load_lds_dwordx4 v128, s[8:9] sc1
	s_mov_b32 m0, s40
	s_mov_b64 s[14:15], 0x80
	v_lshl_add_u64 v[6:7], s[28:29], 0, v[130:131]
	global_load_lds_dwordx4 v130, s[8:9] sc1
	s_add_i32 m0, s37, 0x18000
	v_lshl_add_u64 v[4:5], v[4:5], 0, s[14:15]
	v_lshl_add_u64 v[8:9], s[30:31], 0, v[128:129]
	global_load_lds_dwordx4 v[4:5], off sc1
	v_lshl_add_u64 v[4:5], v[6:7], 0, s[14:15]
	s_add_i32 m0, s37, 0x1a000
	s_add_i32 s41, s37, 0x8000
	v_lshl_add_u64 v[10:11], s[30:31], 0, v[130:131]
	global_load_lds_dwordx4 v[4:5], off sc1
	v_lshl_add_u64 v[4:5], v[8:9], 0, s[14:15]
	s_mov_b32 m0, s41
	s_add_i32 s42, s37, 0xa000
	global_load_lds_dwordx4 v[4:5], off sc1
	v_lshl_add_u64 v[4:5], v[10:11], 0, s[14:15]
	s_mov_b32 m0, s42
	s_add_u32 s8, s28, 0x380080
	global_load_lds_dwordx4 v[4:5], off sc1
	s_addc_u32 s9, s29, 0
	s_add_i32 m0, s37, 0x1c000
	s_mov_b32 s45, 0
	global_load_lds_dwordx4 v128, s[8:9] sc1
	s_add_i32 m0, s37, 0x1e000
	s_cmp_lg_u32 s16, 1
	global_load_lds_dwordx4 v130, s[8:9] sc1
	s_load_dwordx4 s[8:11], s[0:1], 0x10
	s_waitcnt vmcnt(6)
	s_barrier
	s_cbranch_scc1 .LBB2_7
	s_barrier

.LBB2_20:
	s_add_u32 s30, s28, 0xffc80080
	s_addc_u32 s31, s29, -1
	s_cmpk_eq_i32 s58, 0xdc
	s_cselect_b32 s35, s25, s31
	s_cselect_b32 s34, s24, s30
	s_cselect_b32 s31, s27, s57
	s_cselect_b32 s30, s26, s56
	s_add_i32 m0, s37, 0xc000
	ds_read_b128 v[166:169], v143
	ds_read_b128 v[170:173], v147
	ds_read_b128 v[174:177], v149
	ds_read_b128 v[178:181], v150
	ds_read_b128 v[182:185], v151
	ds_read_b128 v[186:189], v152
	ds_read_b128 v[190:193], v153
	ds_read_b128 v[194:197], v154
	ds_read_b128 v[198:201], v155
	ds_read_b128 v[202:205], v155 offset:2048
	ds_read_b128 v[206:209], v156
	ds_read_b128 v[210:213], v156 offset:2048
	ds_read_b128 v[214:217], v155 offset:4096
	ds_read_b128 v[218:221], v155 offset:6144
	ds_read_b128 v[222:225], v156 offset:4096
	ds_read_b128 v[226:229], v156 offset:6144
	global_load_lds_dwordx4 v134, s[28:29] sc1
	s_add_i32 m0, s37, 0xe000
	s_nop 0
	global_load_lds_dwordx4 v132, s[28:29] sc1
	s_waitcnt vmcnt(8)
	s_waitcnt lgkmcnt(0)
	s_barrier
	s_setprio 1
	s_waitcnt lgkmcnt(0)
	v_mfma_f32_16x16x32_f16 v[124:127], v[166:169], v[198:201], v[124:127]
	v_mfma_f32_16x16x32_f16 v[124:127], v[170:173], v[206:209], v[124:127]
	v_mfma_f32_16x16x32_f16 v[120:123], v[178:181], v[206:209], v[120:123]
	v_mfma_f32_16x16x32_f16 v[120:123], v[174:177], v[198:201], v[120:123]
	v_mfma_f32_16x16x32_f16 v[112:115], v[174:177], v[202:205], v[112:115]
	v_mfma_f32_16x16x32_f16 v[112:115], v[178:181], v[210:213], v[112:115]
	v_mfma_f32_16x16x32_f16 v[116:119], v[170:173], v[210:213], v[116:119]
	v_mfma_f32_16x16x32_f16 v[116:119], v[166:169], v[202:205], v[116:119]
	v_mfma_f32_16x16x32_f16 v[108:111], v[166:169], v[214:217], v[108:111]
	v_mfma_f32_16x16x32_f16 v[108:111], v[170:173], v[222:225], v[108:111]
	v_mfma_f32_16x16x32_f16 v[100:103], v[178:181], v[222:225], v[100:103]
	v_mfma_f32_16x16x32_f16 v[100:103], v[174:177], v[214:217], v[100:103]
	v_mfma_f32_16x16x32_f16 v[84:87], v[174:177], v[218:221], v[84:87]
	v_mfma_f32_16x16x32_f16 v[84:87], v[178:181], v[226:229], v[84:87]
	v_mfma_f32_16x16x32_f16 v[92:95], v[170:173], v[226:229], v[92:95]
	v_mfma_f32_16x16x32_f16 v[92:95], v[166:169], v[218:221], v[92:95]
	s_setprio 0
	s_setprio 1
	v_mfma_f32_16x16x32_f16 v[104:107], v[182:185], v[198:201], v[104:107]
	v_mfma_f32_16x16x32_f16 v[104:107], v[186:189], v[206:209], v[104:107]
	v_mfma_f32_16x16x32_f16 v[96:99], v[194:197], v[206:209], v[96:99]
	v_mfma_f32_16x16x32_f16 v[96:99], v[190:193], v[198:201], v[96:99]
	v_mfma_f32_16x16x32_f16 v[80:83], v[190:193], v[202:205], v[80:83]
	v_mfma_f32_16x16x32_f16 v[80:83], v[194:197], v[210:213], v[80:83]
	v_mfma_f32_16x16x32_f16 v[88:91], v[186:189], v[210:213], v[88:91]
	v_mfma_f32_16x16x32_f16 v[88:91], v[182:185], v[202:205], v[88:91]
	v_mfma_f32_16x16x32_f16 v[76:79], v[182:185], v[214:217], v[76:79]
	v_mfma_f32_16x16x32_f16 v[76:79], v[186:189], v[222:225], v[76:79]
	v_mfma_f32_16x16x32_f16 v[72:75], v[194:197], v[222:225], v[72:75]
	v_mfma_f32_16x16x32_f16 v[72:75], v[190:193], v[214:217], v[72:75]
	v_mfma_f32_16x16x32_f16 v[64:67], v[190:193], v[218:221], v[64:67]
	v_mfma_f32_16x16x32_f16 v[64:67], v[194:197], v[226:229], v[64:67]
	v_mfma_f32_16x16x32_f16 v[68:71], v[186:189], v[226:229], v[68:71]
	v_mfma_f32_16x16x32_f16 v[68:71], v[182:185], v[218:221], v[68:71]
	s_setprio 0
	s_barrier
	s_add_i32 s59, s43, s36
	s_mov_b32 m0, s59
	ds_read_b128 v[198:201], v155 offset:16384
	ds_read_b128 v[202:205], v155 offset:18432
	ds_read_b128 v[206:209], v156 offset:16384
	ds_read_b128 v[210:213], v156 offset:18432
	ds_read_b128 v[214:217], v155 offset:20480
	ds_read_b128 v[218:221], v155 offset:22528
	ds_read_b128 v[222:225], v156 offset:20480
	ds_read_b128 v[226:229], v156 offset:22528
	global_load_lds_dwordx4 v128, s[30:31] sc1
	s_add_i32 m0, s59, 0x2000
	s_add_u32 s60, s30, 0x380000
	s_addc_u32 s61, s31, 0
	s_add_i32 s59, s44, s36
	global_load_lds_dwordx4 v130, s[30:31] sc1
	s_mov_b32 m0, s59
	s_add_u32 s62, s30, 0x80
	s_addc_u32 s63, s31, 0
	global_load_lds_dwordx4 v128, s[60:61] sc1
	s_add_i32 m0, s59, 0x2000
	s_add_u32 s64, s34, 0x80
	s_addc_u32 s65, s35, 0
	global_load_lds_dwordx4 v130, s[60:61] sc1
	s_mov_b32 m0, s37
	s_nop 0
	global_load_lds_dwordx4 v128, s[34:35] sc1
	s_mov_b32 m0, s38
	s_nop 0
	global_load_lds_dwordx4 v130, s[34:35] sc1
	s_waitcnt vmcnt(8)
	s_waitcnt lgkmcnt(0)
	s_barrier
	s_setprio 1
	s_waitcnt lgkmcnt(0)
	v_mfma_f32_16x16x32_f16 v[60:63], v[166:169], v[198:201], v[60:63]
	v_mfma_f32_16x16x32_f16 v[60:63], v[170:173], v[206:209], v[60:63]
	v_mfma_f32_16x16x32_f16 v[56:59], v[178:181], v[206:209], v[56:59]
	v_mfma_f32_16x16x32_f16 v[56:59], v[174:177], v[198:201], v[56:59]
	v_mfma_f32_16x16x32_f16 v[48:51], v[174:177], v[202:205], v[48:51]
	v_mfma_f32_16x16x32_f16 v[48:51], v[178:181], v[210:213], v[48:51]
	v_mfma_f32_16x16x32_f16 v[52:55], v[170:173], v[210:213], v[52:55]
	v_mfma_f32_16x16x32_f16 v[52:55], v[166:169], v[202:205], v[52:55]
	v_mfma_f32_16x16x32_f16 v[40:43], v[166:169], v[214:217], v[40:43]
	v_mfma_f32_16x16x32_f16 v[40:43], v[170:173], v[222:225], v[40:43]
	v_mfma_f32_16x16x32_f16 v[32:35], v[178:181], v[222:225], v[32:35]
	v_mfma_f32_16x16x32_f16 v[32:35], v[174:177], v[214:217], v[32:35]
	v_mfma_f32_16x16x32_f16 v[8:11], v[174:177], v[218:221], v[8:11]
	v_mfma_f32_16x16x32_f16 v[8:11], v[178:181], v[226:229], v[8:11]
	v_mfma_f32_16x16x32_f16 v[12:15], v[170:173], v[226:229], v[12:15]
	v_mfma_f32_16x16x32_f16 v[12:15], v[166:169], v[218:221], v[12:15]
	s_setprio 0
	s_setprio 1
	v_mfma_f32_16x16x32_f16 v[44:47], v[182:185], v[198:201], v[44:47]
	v_mfma_f32_16x16x32_f16 v[44:47], v[186:189], v[206:209], v[44:47]
	v_mfma_f32_16x16x32_f16 v[36:39], v[194:197], v[206:209], v[36:39]
	v_mfma_f32_16x16x32_f16 v[36:39], v[190:193], v[198:201], v[36:39]
	v_mfma_f32_16x16x32_f16 v[24:27], v[190:193], v[202:205], v[24:27]
	v_mfma_f32_16x16x32_f16 v[24:27], v[194:197], v[210:213], v[24:27]
	v_mfma_f32_16x16x32_f16 v[28:31], v[186:189], v[210:213], v[28:31]
	v_mfma_f32_16x16x32_f16 v[28:31], v[182:185], v[202:205], v[28:31]
	v_mfma_f32_16x16x32_f16 v[20:23], v[182:185], v[214:217], v[20:23]
	v_mfma_f32_16x16x32_f16 v[20:23], v[186:189], v[222:225], v[20:23]
	v_mfma_f32_16x16x32_f16 v[16:19], v[194:197], v[222:225], v[16:19]
	v_mfma_f32_16x16x32_f16 v[16:19], v[190:193], v[214:217], v[16:19]
	v_mfma_f32_16x16x32_f16 v[0:3], v[190:193], v[218:221], v[0:3]
	v_mfma_f32_16x16x32_f16 v[0:3], v[194:197], v[226:229], v[0:3]
	v_mfma_f32_16x16x32_f16 v[4:7], v[186:189], v[226:229], v[4:7]
	v_mfma_f32_16x16x32_f16 v[4:7], v[182:185], v[218:221], v[4:7]
	s_setprio 0
	s_barrier
	s_add_u32 s34, s34, 0x380000
	s_addc_u32 s35, s35, 0
	s_mov_b32 m0, s39
	ds_read_b128 v[166:169], v157
	ds_read_b128 v[170:173], v158
	ds_read_b128 v[174:177], v159
	ds_read_b128 v[178:181], v160
	ds_read_b128 v[182:185], v161
	ds_read_b128 v[186:189], v162
	ds_read_b128 v[190:193], v163
	ds_read_b128 v[194:197], v164
	ds_read_b128 v[198:201], v155 offset:32768
	ds_read_b128 v[202:205], v155 offset:34816
	ds_read_b128 v[206:209], v156 offset:32768
	ds_read_b128 v[210:213], v156 offset:34816
	ds_read_b128 v[214:217], v155 offset:36864
	ds_read_b128 v[218:221], v155 offset:38912
	ds_read_b128 v[222:225], v156 offset:36864
	ds_read_b128 v[226:229], v156 offset:38912
	global_load_lds_dwordx4 v128, s[34:35] sc1
	s_mov_b32 m0, s40
	s_nop 0
	global_load_lds_dwordx4 v130, s[34:35] sc1
	s_waitcnt vmcnt(8)
	s_waitcnt lgkmcnt(0)
	s_barrier
	s_setprio 1
	s_waitcnt lgkmcnt(0)
	v_mfma_f32_16x16x32_f16 v[124:127], v[166:169], v[198:201], v[124:127]
	v_mfma_f32_16x16x32_f16 v[124:127], v[170:173], v[206:209], v[124:127]
	v_mfma_f32_16x16x32_f16 v[120:123], v[178:181], v[206:209], v[120:123]
	v_mfma_f32_16x16x32_f16 v[120:123], v[174:177], v[198:201], v[120:123]
	v_mfma_f32_16x16x32_f16 v[112:115], v[174:177], v[202:205], v[112:115]
	v_mfma_f32_16x16x32_f16 v[112:115], v[178:181], v[210:213], v[112:115]
	v_mfma_f32_16x16x32_f16 v[116:119], v[170:173], v[210:213], v[116:119]
	v_mfma_f32_16x16x32_f16 v[116:119], v[166:169], v[202:205], v[116:119]
	v_mfma_f32_16x16x32_f16 v[108:111], v[166:169], v[214:217], v[108:111]
	v_mfma_f32_16x16x32_f16 v[108:111], v[170:173], v[222:225], v[108:111]
	v_mfma_f32_16x16x32_f16 v[100:103], v[178:181], v[222:225], v[100:103]
	v_mfma_f32_16x16x32_f16 v[100:103], v[174:177], v[214:217], v[100:103]
	v_mfma_f32_16x16x32_f16 v[84:87], v[174:177], v[218:221], v[84:87]
	v_mfma_f32_16x16x32_f16 v[84:87], v[178:181], v[226:229], v[84:87]
	v_mfma_f32_16x16x32_f16 v[92:95], v[170:173], v[226:229], v[92:95]
	v_mfma_f32_16x16x32_f16 v[92:95], v[166:169], v[218:221], v[92:95]
	s_setprio 0
	s_setprio 1
	v_mfma_f32_16x16x32_f16 v[104:107], v[182:185], v[198:201], v[104:107]
	v_mfma_f32_16x16x32_f16 v[104:107], v[186:189], v[206:209], v[104:107]
	v_mfma_f32_16x16x32_f16 v[96:99], v[194:197], v[206:209], v[96:99]
	v_mfma_f32_16x16x32_f16 v[96:99], v[190:193], v[198:201], v[96:99]
	v_mfma_f32_16x16x32_f16 v[80:83], v[190:193], v[202:205], v[80:83]
	v_mfma_f32_16x16x32_f16 v[80:83], v[194:197], v[210:213], v[80:83]
	v_mfma_f32_16x16x32_f16 v[88:91], v[186:189], v[210:213], v[88:91]
	v_mfma_f32_16x16x32_f16 v[88:91], v[182:185], v[202:205], v[88:91]
	v_mfma_f32_16x16x32_f16 v[76:79], v[182:185], v[214:217], v[76:79]
	v_mfma_f32_16x16x32_f16 v[76:79], v[186:189], v[222:225], v[76:79]
	v_mfma_f32_16x16x32_f16 v[72:75], v[194:197], v[222:225], v[72:75]
	v_mfma_f32_16x16x32_f16 v[72:75], v[190:193], v[214:217], v[72:75]
	v_mfma_f32_16x16x32_f16 v[64:67], v[190:193], v[218:221], v[64:67]
	v_mfma_f32_16x16x32_f16 v[64:67], v[194:197], v[226:229], v[64:67]
	v_mfma_f32_16x16x32_f16 v[68:71], v[186:189], v[226:229], v[68:71]
	v_mfma_f32_16x16x32_f16 v[68:71], v[182:185], v[218:221], v[68:71]
	s_setprio 0
	s_barrier
	s_add_i32 s34, s46, s36
	s_mov_b32 m0, s34
	ds_read_b128 v[198:201], v155 offset:49152
	ds_read_b128 v[202:205], v155 offset:51200
	ds_read_b128 v[206:209], v156 offset:49152
	ds_read_b128 v[210:213], v156 offset:51200
	ds_read_b128 v[214:217], v155 offset:53248
	ds_read_b128 v[218:221], v155 offset:55296
	ds_read_b128 v[222:225], v156 offset:53248
	ds_read_b128 v[226:229], v156 offset:55296
	global_load_lds_dwordx4 v128, s[62:63] sc1
	s_add_i32 m0, s34, 0x2000
	s_add_u32 s30, s30, 0x380080
	s_addc_u32 s31, s31, 0
	s_add_i32 s34, s47, s36
	global_load_lds_dwordx4 v130, s[62:63] sc1
	s_mov_b32 m0, s34
	s_nop 0
	global_load_lds_dwordx4 v128, s[30:31] sc1
	s_add_i32 m0, s34, 0x2000
	s_nop 0
	global_load_lds_dwordx4 v130, s[30:31] sc1
	s_mov_b32 m0, s41
	s_nop 0
	global_load_lds_dwordx4 v128, s[64:65] sc1
	s_mov_b32 m0, s42
	s_nop 0
	global_load_lds_dwordx4 v130, s[64:65] sc1
	s_waitcnt vmcnt(8)
	s_waitcnt lgkmcnt(0)
	s_barrier
	s_setprio 1
	s_waitcnt lgkmcnt(0)
	v_mfma_f32_16x16x32_f16 v[60:63], v[166:169], v[198:201], v[60:63]
	v_mfma_f32_16x16x32_f16 v[60:63], v[170:173], v[206:209], v[60:63]
	v_mfma_f32_16x16x32_f16 v[56:59], v[178:181], v[206:209], v[56:59]
	v_mfma_f32_16x16x32_f16 v[56:59], v[174:177], v[198:201], v[56:59]
	v_mfma_f32_16x16x32_f16 v[48:51], v[174:177], v[202:205], v[48:51]
	v_mfma_f32_16x16x32_f16 v[48:51], v[178:181], v[210:213], v[48:51]
	v_mfma_f32_16x16x32_f16 v[52:55], v[170:173], v[210:213], v[52:55]
	v_mfma_f32_16x16x32_f16 v[52:55], v[166:169], v[202:205], v[52:55]
	v_mfma_f32_16x16x32_f16 v[40:43], v[166:169], v[214:217], v[40:43]
	v_mfma_f32_16x16x32_f16 v[40:43], v[170:173], v[222:225], v[40:43]
	v_mfma_f32_16x16x32_f16 v[32:35], v[178:181], v[222:225], v[32:35]
	v_mfma_f32_16x16x32_f16 v[32:35], v[174:177], v[214:217], v[32:35]
	v_mfma_f32_16x16x32_f16 v[8:11], v[174:177], v[218:221], v[8:11]
	v_mfma_f32_16x16x32_f16 v[8:11], v[178:181], v[226:229], v[8:11]
	v_mfma_f32_16x16x32_f16 v[12:15], v[170:173], v[226:229], v[12:15]
	v_mfma_f32_16x16x32_f16 v[12:15], v[166:169], v[218:221], v[12:15]
	s_setprio 0
	s_setprio 1
	v_mfma_f32_16x16x32_f16 v[44:47], v[182:185], v[198:201], v[44:47]
	v_mfma_f32_16x16x32_f16 v[44:47], v[186:189], v[206:209], v[44:47]
	v_mfma_f32_16x16x32_f16 v[36:39], v[194:197], v[206:209], v[36:39]
	v_mfma_f32_16x16x32_f16 v[36:39], v[190:193], v[198:201], v[36:39]
	v_mfma_f32_16x16x32_f16 v[24:27], v[190:193], v[202:205], v[24:27]
	v_mfma_f32_16x16x32_f16 v[24:27], v[194:197], v[210:213], v[24:27]
	v_mfma_f32_16x16x32_f16 v[28:31], v[186:189], v[210:213], v[28:31]
	v_mfma_f32_16x16x32_f16 v[28:31], v[182:185], v[202:205], v[28:31]
	v_mfma_f32_16x16x32_f16 v[20:23], v[182:185], v[214:217], v[20:23]
	v_mfma_f32_16x16x32_f16 v[20:23], v[186:189], v[222:225], v[20:23]
	v_mfma_f32_16x16x32_f16 v[16:19], v[194:197], v[222:225], v[16:19]
	v_mfma_f32_16x16x32_f16 v[16:19], v[190:193], v[214:217], v[16:19]
	v_mfma_f32_16x16x32_f16 v[0:3], v[190:193], v[218:221], v[0:3]
	v_mfma_f32_16x16x32_f16 v[0:3], v[194:197], v[226:229], v[0:3]
	v_mfma_f32_16x16x32_f16 v[4:7], v[186:189], v[226:229], v[4:7]
	v_mfma_f32_16x16x32_f16 v[4:7], v[182:185], v[218:221], v[4:7]
	s_setprio 0
	s_barrier
	s_add_i32 s58, s58, 2
	s_add_u32 s56, s56, 0x100
	s_addc_u32 s57, s57, 0
	s_add_u32 s28, s28, 0x100
	s_addc_u32 s29, s29, 0
	s_cmpk_gt_u32 s58, 0xdd
	s_cbranch_scc0 .LBB2_20
	v_lshl_add_u32 v144, s55, 8, v137
	v_ashrrev_i32_e32 v145, 31, v144
	v_lshl_add_u64 v[138:139], v[144:145], 2, s[10:11]
	global_load_dword v136, v[138:139], off
	global_load_dword v140, v[138:139], off offset:64
	global_load_dword v142, v[138:139], off offset:128
	global_load_dword v146, v[138:139], off offset:192
	global_load_dword v148, v[138:139], off offset:512
	global_load_dword v174, v[138:139], off offset:576
	global_load_dword v176, v[138:139], off offset:640
	s_nop 0
	global_load_dword v138, v[138:139], off offset:704
	v_lshl_or_b32 v166, s54, 8, v141
	v_ashrrev_i32_e32 v167, 31, v166
	v_or_b32_e32 v168, 16, v144
	v_or_b32_e32 v170, 32, v144
	v_or_b32_e32 v172, 48, v144
	v_lshl_add_u64 v[166:167], v[166:167], 2, s[8:9]
	v_lshlrev_b64 v[144:145], 14, v[144:145]
	v_ashrrev_i32_e32 v169, 31, v168
	v_ashrrev_i32_e32 v171, 31, v170
	v_ashrrev_i32_e32 v173, 31, v172
	v_lshl_add_u64 v[144:145], v[166:167], 0, v[144:145]
	v_lshlrev_b64 v[168:169], 14, v[168:169]
	v_lshlrev_b64 v[170:171], 14, v[170:171]
	v_lshlrev_b64 v[172:173], 14, v[172:173]
	v_add_co_u32_e32 v178, vcc, s48, v144
	v_lshl_add_u64 v[168:169], v[166:167], 0, v[168:169]
	v_lshl_add_u64 v[170:171], v[166:167], 0, v[170:171]
	v_lshl_add_u64 v[166:167], v[166:167], 0, v[172:173]
	v_lshl_add_u64 v[172:173], v[144:145], 0, s[16:17]
	v_addc_co_u32_e32 v179, vcc, 0, v145, vcc
	s_mov_b32 s55, s45
	s_mov_b32 s54, s53
	s_mov_b64 s[28:29], s[26:27]
	s_mov_b64 s[30:31], s[24:25]
	s_waitcnt vmcnt(0)
	v_pk_mul_f32 v[126:127], v[136:137], v[126:127] op_sel_hi:[0,1]
	v_pk_mul_f32 v[124:125], v[136:137], v[124:125] op_sel_hi:[0,1]
	v_pk_mul_f32 v[122:123], v[136:137], v[122:123] op_sel_hi:[0,1]
	v_pk_mul_f32 v[120:121], v[136:137], v[120:121] op_sel_hi:[0,1]
	v_pk_mul_f32 v[46:47], v[148:149], v[46:47] op_sel_hi:[0,1]
	v_pk_mul_f32 v[44:45], v[148:149], v[44:45] op_sel_hi:[0,1]
	v_pk_mul_f32 v[106:107], v[136:137], v[106:107] op_sel_hi:[0,1]
	v_pk_mul_f32 v[104:105], v[136:137], v[104:105] op_sel_hi:[0,1]
	v_pk_mul_f32 v[98:99], v[136:137], v[98:99] op_sel_hi:[0,1]
	v_pk_mul_f32 v[96:97], v[136:137], v[96:97] op_sel_hi:[0,1]
	v_pk_mul_f32 v[118:119], v[140:141], v[118:119] op_sel_hi:[0,1]
	v_pk_mul_f32 v[116:117], v[140:141], v[116:117] op_sel_hi:[0,1]
	v_pk_mul_f32 v[114:115], v[140:141], v[114:115] op_sel_hi:[0,1]
	v_pk_mul_f32 v[112:113], v[140:141], v[112:113] op_sel_hi:[0,1]
	v_pk_mul_f32 v[90:91], v[140:141], v[90:91] op_sel_hi:[0,1]
	v_pk_mul_f32 v[88:89], v[140:141], v[88:89] op_sel_hi:[0,1]
	v_pk_mul_f32 v[82:83], v[140:141], v[82:83] op_sel_hi:[0,1]
	v_pk_mul_f32 v[80:81], v[140:141], v[80:81] op_sel_hi:[0,1]
	v_pk_mul_f32 v[110:111], v[142:143], v[110:111] op_sel_hi:[0,1]
	v_pk_mul_f32 v[108:109], v[142:143], v[108:109] op_sel_hi:[0,1]
	v_pk_mul_f32 v[102:103], v[142:143], v[102:103] op_sel_hi:[0,1]
	v_pk_mul_f32 v[100:101], v[142:143], v[100:101] op_sel_hi:[0,1]
	v_pk_mul_f32 v[78:79], v[142:143], v[78:79] op_sel_hi:[0,1]
	v_pk_mul_f32 v[76:77], v[142:143], v[76:77] op_sel_hi:[0,1]
	v_pk_mul_f32 v[74:75], v[142:143], v[74:75] op_sel_hi:[0,1]
	v_pk_mul_f32 v[72:73], v[142:143], v[72:73] op_sel_hi:[0,1]
	v_pk_mul_f32 v[94:95], v[146:147], v[94:95] op_sel_hi:[0,1]
	v_pk_mul_f32 v[92:93], v[146:147], v[92:93] op_sel_hi:[0,1]
	v_pk_mul_f32 v[86:87], v[146:147], v[86:87] op_sel_hi:[0,1]
	v_pk_mul_f32 v[84:85], v[146:147], v[84:85] op_sel_hi:[0,1]
	v_pk_mul_f32 v[70:71], v[146:147], v[70:71] op_sel_hi:[0,1]
	v_pk_mul_f32 v[68:69], v[146:147], v[68:69] op_sel_hi:[0,1]
	v_pk_mul_f32 v[66:67], v[146:147], v[66:67] op_sel_hi:[0,1]
	v_pk_mul_f32 v[64:65], v[146:147], v[64:65] op_sel_hi:[0,1]
	v_pk_mul_f32 v[62:63], v[148:149], v[62:63] op_sel_hi:[0,1]
	v_pk_mul_f32 v[60:61], v[148:149], v[60:61] op_sel_hi:[0,1]
	global_store_dwordx4 v[144:145], v[124:127], off
	global_store_dwordx4 v[144:145], v[120:123], off offset:64
	global_store_dwordx4 v[144:145], v[104:107], off offset:512
	global_store_dwordx4 v[144:145], v[96:99], off offset:576
	global_store_dwordx4 v[168:169], v[116:119], off
	global_store_dwordx4 v[168:169], v[112:115], off offset:64
	global_store_dwordx4 v[168:169], v[88:91], off offset:512
	global_store_dwordx4 v[168:169], v[80:83], off offset:576
	global_store_dwordx4 v[170:171], v[108:111], off
	global_store_dwordx4 v[170:171], v[100:103], off offset:64
	global_store_dwordx4 v[170:171], v[76:79], off offset:512
	global_store_dwordx4 v[170:171], v[72:75], off offset:576
	global_store_dwordx4 v[166:167], v[92:95], off
	global_store_dwordx4 v[166:167], v[84:87], off offset:64
	global_store_dwordx4 v[166:167], v[68:71], off offset:512
	global_store_dwordx4 v[166:167], v[64:67], off offset:576
	global_store_dwordx4 v[178:179], v[60:63], off
	global_store_dwordx4 v[172:173], v[44:47], off offset:512
	v_pk_mul_f32 v[30:31], v[174:175], v[30:31] op_sel_hi:[0,1]
	v_pk_mul_f32 v[28:29], v[174:175], v[28:29] op_sel_hi:[0,1]
	v_add_co_u32_e32 v46, vcc, s49, v144
	v_lshl_add_u64 v[44:45], v[144:145], 0, s[18:19]
	s_nop 0
	v_addc_co_u32_e32 v47, vcc, 0, v145, vcc
	global_store_dwordx4 v[44:45], v[28:31], off offset:512
	v_pk_mul_f32 v[18:19], v[176:177], v[18:19] op_sel_hi:[0,1]
	v_pk_mul_f32 v[16:17], v[176:177], v[16:17] op_sel_hi:[0,1]
	v_add_co_u32_e32 v30, vcc, s50, v144
	v_lshl_add_u64 v[28:29], v[144:145], 0, s[20:21]
	s_nop 0
	v_addc_co_u32_e32 v31, vcc, 0, v145, vcc
	v_pk_mul_f32 v[38:39], v[148:149], v[38:39] op_sel_hi:[0,1]
	v_pk_mul_f32 v[36:37], v[148:149], v[36:37] op_sel_hi:[0,1]
	v_pk_mul_f32 v[26:27], v[174:175], v[26:27] op_sel_hi:[0,1]
	v_pk_mul_f32 v[24:25], v[174:175], v[24:25] op_sel_hi:[0,1]
	global_store_dwordx4 v[28:29], v[16:19], off offset:576
	global_store_dwordx4 v[172:173], v[36:39], off offset:576
	global_store_dwordx4 v[44:45], v[24:27], off offset:576
	v_add_co_u32_e32 v18, vcc, s51, v144
	v_pk_mul_f32 v[38:39], v[174:175], v[54:55] op_sel_hi:[0,1]
	v_pk_mul_f32 v[36:37], v[174:175], v[52:53] op_sel_hi:[0,1]
	v_pk_mul_f32 v[26:27], v[176:177], v[42:43] op_sel_hi:[0,1]
	v_pk_mul_f32 v[24:25], v[176:177], v[40:41] op_sel_hi:[0,1]
	v_addc_co_u32_e32 v19, vcc, 0, v145, vcc
	v_pk_mul_f32 v[58:59], v[148:149], v[58:59] op_sel_hi:[0,1]
	v_pk_mul_f32 v[56:57], v[148:149], v[56:57] op_sel_hi:[0,1]
	global_store_dwordx4 v[46:47], v[36:39], off
	global_store_dwordx4 v[30:31], v[24:27], off
	v_pk_mul_f32 v[22:23], v[176:177], v[22:23] op_sel_hi:[0,1]
	v_pk_mul_f32 v[38:39], v[174:175], v[50:51] op_sel_hi:[0,1]
	v_pk_mul_f32 v[36:37], v[174:175], v[48:49] op_sel_hi:[0,1]
	v_pk_mul_f32 v[26:27], v[176:177], v[34:35] op_sel_hi:[0,1]
	v_pk_mul_f32 v[24:25], v[176:177], v[32:33] op_sel_hi:[0,1]
	v_pk_mul_f32 v[20:21], v[176:177], v[20:21] op_sel_hi:[0,1]
	v_lshl_add_u64 v[16:17], v[144:145], 0, s[22:23]
	v_pk_mul_f32 v[14:15], v[138:139], v[14:15] op_sel_hi:[0,1]
	v_pk_mul_f32 v[12:13], v[138:139], v[12:13] op_sel_hi:[0,1]
	v_pk_mul_f32 v[10:11], v[138:139], v[10:11] op_sel_hi:[0,1]
	v_pk_mul_f32 v[8:9], v[138:139], v[8:9] op_sel_hi:[0,1]
	v_pk_mul_f32 v[6:7], v[138:139], v[6:7] op_sel_hi:[0,1]
	v_pk_mul_f32 v[4:5], v[138:139], v[4:5] op_sel_hi:[0,1]
	v_pk_mul_f32 v[2:3], v[138:139], v[2:3] op_sel_hi:[0,1]
	v_pk_mul_f32 v[0:1], v[138:139], v[0:1] op_sel_hi:[0,1]
	s_mov_b64 vcc, s[0:1]
	global_store_dwordx4 v[172:173], v[56:59], off offset:64
	global_store_dwordx4 v[44:45], v[36:39], off offset:64
	global_store_dwordx4 v[28:29], v[24:27], off offset:64
	global_store_dwordx4 v[28:29], v[20:23], off offset:512
	global_store_dwordx4 v[18:19], v[12:15], off
	global_store_dwordx4 v[16:17], v[8:11], off offset:64
	global_store_dwordx4 v[16:17], v[4:7], off offset:512
	global_store_dwordx4 v[16:17], v[0:3], off offset:576
	s_cbranch_vccz .LBB2_8
	s_waitcnt vmcnt(0)
	s_cmpk_gt_u32 s33, 0xff
	s_cbranch_scc1 .LBB2_24
	s_barrier
